# per-block phase-B barrier placed after issuing the delta read (LDS latency overlaps the barrier wait)
# speedup vs baseline: 1.0375x; 1.0073x over previous
.LBB0_3:
	ds_read_b128 v[70:73], v203
	v_add_u32_e32 v132, s12, v220
	s_add_i32 s12, s12, 0x2000000
	v_add_u32_e32 v203, 0x400, v203
	s_cmp_eq_u32 s12, 0x10000000
	s_barrier
	s_waitcnt lgkmcnt(0)
	v_mfma_f32_16x16x32_bf16 v[66:69], v[144:147], v[70:73], 0
	v_add_u32_e32 v133, 0x4000, v132
	v_add_u32_e32 v134, 0x8000, v132
	v_add_u32_e32 v135, 0xc000, v132
	v_mfma_f32_16x16x32_bf16 v[74:77], v[148:151], v[70:73], 0
	v_add_u32_e32 v136, 0x10000, v132
	s_nop 2
	v_exp_f32_e32 v66, v66
	v_exp_f32_e32 v67, v67
	v_mfma_f32_16x16x32_bf16 v[78:81], v[152:155], v[70:73], 0
	v_exp_f32_e32 v68, v68
	v_exp_f32_e32 v69, v69
	v_exp_f32_e32 v74, v74
	v_mfma_f32_16x16x32_bf16 v[82:85], v[156:159], v[70:73], 0
	v_exp_f32_e32 v75, v75
	v_exp_f32_e32 v76, v76
	v_exp_f32_e32 v77, v77
	v_mfma_f32_16x16x32_bf16 v[86:89], v[160:163], v[70:73], 0
	v_exp_f32_e32 v78, v78
	v_exp_f32_e32 v79, v79
	v_exp_f32_e32 v80, v80
	v_mfma_f32_16x16x32_bf16 v[90:93], v[164:167], v[70:73], 0
	v_exp_f32_e32 v81, v81
	v_exp_f32_e32 v82, v82
	v_exp_f32_e32 v83, v83
	v_mfma_f32_16x16x32_bf16 v[94:97], v[168:171], v[70:73], 0
	v_exp_f32_e32 v84, v84
	v_exp_f32_e32 v85, v85
	v_exp_f32_e32 v86, v86
	v_mfma_f32_16x16x32_bf16 v[98:101], v[172:175], v[70:73], 0
	v_exp_f32_e32 v87, v87
	v_exp_f32_e32 v88, v88
	v_exp_f32_e32 v89, v89
	v_mfma_f32_16x16x32_bf16 v[102:105], v[176:179], v[70:73], 0
	v_exp_f32_e32 v90, v90
	v_exp_f32_e32 v91, v91
	v_exp_f32_e32 v92, v92
	v_mfma_f32_16x16x32_bf16 v[108:111], v[180:183], v[70:73], 0
	v_exp_f32_e32 v93, v93
	v_exp_f32_e32 v94, v94
	v_exp_f32_e32 v95, v95
	v_mfma_f32_16x16x32_bf16 v[112:115], v[184:187], v[70:73], 0
	v_exp_f32_e32 v96, v96
	v_exp_f32_e32 v97, v97
	v_exp_f32_e32 v98, v98
	v_mfma_f32_16x16x32_bf16 v[116:119], v[188:191], v[70:73], 0
	v_exp_f32_e32 v99, v99
	v_exp_f32_e32 v100, v100
	v_exp_f32_e32 v101, v101
	v_mfma_f32_16x16x32_bf16 v[120:123], v[232:235], v[70:73], 0
	v_exp_f32_e32 v102, v102
	v_exp_f32_e32 v103, v103
	v_exp_f32_e32 v104, v104
	v_mfma_f32_16x16x32_bf16 v[124:127], v[236:239], v[70:73], 0
	v_exp_f32_e32 v105, v105
	v_exp_f32_e32 v108, v108
	v_exp_f32_e32 v109, v109
	v_mfma_f32_16x16x32_bf16 v[128:131], v[240:243], v[70:73], 0
	v_exp_f32_e32 v110, v110
	v_exp_f32_e32 v111, v111
	v_exp_f32_e32 v112, v112
	v_mfma_f32_16x16x32_bf16 v[70:73], v[244:247], v[70:73], 0
	v_exp_f32_e32 v113, v113
	v_exp_f32_e32 v114, v114
	v_exp_f32_e32 v115, v115
	v_exp_f32_e32 v116, v116
	v_exp_f32_e32 v117, v117
	v_exp_f32_e32 v118, v118
	v_exp_f32_e32 v119, v119
	v_exp_f32_e32 v120, v120
	v_exp_f32_e32 v121, v121
	v_exp_f32_e32 v122, v122
	v_exp_f32_e32 v123, v123
	v_exp_f32_e32 v124, v124
	v_exp_f32_e32 v125, v125
	v_exp_f32_e32 v126, v126
	v_exp_f32_e32 v127, v127
	v_exp_f32_e32 v128, v128
	v_exp_f32_e32 v129, v129
	v_exp_f32_e32 v130, v130
	v_exp_f32_e32 v131, v131
	v_exp_f32_e32 v70, v70
	v_exp_f32_e32 v71, v71
	v_exp_f32_e32 v72, v72
	v_exp_f32_e32 v73, v73
	v_pk_add_f32 v[66:67], v[66:67], 1.0 op_sel_hi:[1,0]
	v_pk_add_f32 v[68:69], v[68:69], 1.0 op_sel_hi:[1,0]
	v_pk_add_f32 v[74:75], v[74:75], 1.0 op_sel_hi:[1,0]
	v_pk_add_f32 v[76:77], v[76:77], 1.0 op_sel_hi:[1,0]
	v_pk_add_f32 v[78:79], v[78:79], 1.0 op_sel_hi:[1,0]
	v_pk_add_f32 v[80:81], v[80:81], 1.0 op_sel_hi:[1,0]
	v_pk_add_f32 v[82:83], v[82:83], 1.0 op_sel_hi:[1,0]
	v_pk_add_f32 v[84:85], v[84:85], 1.0 op_sel_hi:[1,0]
	v_pk_add_f32 v[86:87], v[86:87], 1.0 op_sel_hi:[1,0]
	v_pk_add_f32 v[88:89], v[88:89], 1.0 op_sel_hi:[1,0]
	v_pk_add_f32 v[90:91], v[90:91], 1.0 op_sel_hi:[1,0]
	v_pk_add_f32 v[92:93], v[92:93], 1.0 op_sel_hi:[1,0]
	v_pk_add_f32 v[94:95], v[94:95], 1.0 op_sel_hi:[1,0]
	v_pk_add_f32 v[96:97], v[96:97], 1.0 op_sel_hi:[1,0]
	v_pk_add_f32 v[98:99], v[98:99], 1.0 op_sel_hi:[1,0]
	v_pk_add_f32 v[100:101], v[100:101], 1.0 op_sel_hi:[1,0]
	v_pk_add_f32 v[102:103], v[102:103], 1.0 op_sel_hi:[1,0]
	v_pk_add_f32 v[104:105], v[104:105], 1.0 op_sel_hi:[1,0]
	v_rcp_f32_e32 v66, v66
	v_rcp_f32_e32 v67, v67
	v_rcp_f32_e32 v68, v68
	v_rcp_f32_e32 v69, v69
	v_pk_add_f32 v[108:109], v[108:109], 1.0 op_sel_hi:[1,0]
	v_pk_add_f32 v[110:111], v[110:111], 1.0 op_sel_hi:[1,0]
	v_pk_add_f32 v[112:113], v[112:113], 1.0 op_sel_hi:[1,0]
	v_pk_add_f32 v[114:115], v[114:115], 1.0 op_sel_hi:[1,0]
	v_pk_add_f32 v[116:117], v[116:117], 1.0 op_sel_hi:[1,0]
	v_pk_add_f32 v[118:119], v[118:119], 1.0 op_sel_hi:[1,0]
	v_pk_add_f32 v[120:121], v[120:121], 1.0 op_sel_hi:[1,0]
	v_pk_add_f32 v[122:123], v[122:123], 1.0 op_sel_hi:[1,0]
	v_pk_add_f32 v[124:125], v[124:125], 1.0 op_sel_hi:[1,0]
	v_pk_add_f32 v[126:127], v[126:127], 1.0 op_sel_hi:[1,0]
	v_pk_add_f32 v[128:129], v[128:129], 1.0 op_sel_hi:[1,0]
	v_pk_add_f32 v[130:131], v[130:131], 1.0 op_sel_hi:[1,0]
	v_add_f32_e32 v140, 1.0, v70
	v_add_f32_e32 v141, 1.0, v71
	v_add_f32_e32 v142, 1.0, v72
	v_add_f32_e32 v143, 1.0, v73
	v_rcp_f32_e32 v70, v74
	v_rcp_f32_e32 v71, v75
	v_rcp_f32_e32 v72, v76
	v_rcp_f32_e32 v73, v77
	v_rcp_f32_e32 v74, v78
	v_rcp_f32_e32 v75, v79
	v_rcp_f32_e32 v76, v80
	v_rcp_f32_e32 v77, v81
	v_rcp_f32_e32 v78, v82
	v_rcp_f32_e32 v79, v83
	v_rcp_f32_e32 v80, v84
	v_rcp_f32_e32 v81, v85
	v_rcp_f32_e32 v82, v86
	v_rcp_f32_e32 v83, v87
	v_rcp_f32_e32 v84, v88
	v_rcp_f32_e32 v85, v89
	v_rcp_f32_e32 v86, v90
	v_rcp_f32_e32 v87, v91
	v_rcp_f32_e32 v88, v92
	v_rcp_f32_e32 v89, v93
	v_rcp_f32_e32 v90, v94
	v_rcp_f32_e32 v91, v95
	v_rcp_f32_e32 v92, v96
	v_rcp_f32_e32 v93, v97
	v_rcp_f32_e32 v94, v98
	v_rcp_f32_e32 v95, v99
	v_rcp_f32_e32 v96, v100
	v_rcp_f32_e32 v97, v101
	v_rcp_f32_e32 v98, v102
	v_rcp_f32_e32 v99, v103
	v_rcp_f32_e32 v100, v104
	v_rcp_f32_e32 v101, v105
	v_rcp_f32_e32 v102, v108
	v_rcp_f32_e32 v103, v109
	v_rcp_f32_e32 v104, v110
	v_rcp_f32_e32 v105, v111
	v_rcp_f32_e32 v108, v112
	v_rcp_f32_e32 v109, v113
	v_rcp_f32_e32 v110, v114
	v_rcp_f32_e32 v111, v115
	v_rcp_f32_e32 v112, v116
	v_rcp_f32_e32 v113, v117
	v_rcp_f32_e32 v114, v118
	v_rcp_f32_e32 v115, v119
	v_rcp_f32_e32 v116, v120
	v_rcp_f32_e32 v117, v121
	v_rcp_f32_e32 v118, v122
	v_rcp_f32_e32 v119, v123
	v_rcp_f32_e32 v120, v124
	v_rcp_f32_e32 v121, v125
	v_rcp_f32_e32 v122, v126
	v_rcp_f32_e32 v123, v127
	v_rcp_f32_e32 v124, v128
	v_rcp_f32_e32 v125, v129
	v_rcp_f32_e32 v126, v130
	v_rcp_f32_e32 v127, v131
	v_rcp_f32_e32 v128, v140
	v_rcp_f32_e32 v129, v141
	v_rcp_f32_e32 v130, v142
	v_rcp_f32_e32 v131, v143
	v_pk_fma_f32 v[66:67], v[66:67], -2.0, 1.0 op_sel_hi:[1,0,0]
	v_pk_fma_f32 v[68:69], v[68:69], -2.0, 1.0 op_sel_hi:[1,0,0]
	v_pk_fma_f32 v[70:71], v[70:71], -2.0, 1.0 op_sel_hi:[1,0,0]
	v_pk_fma_f32 v[72:73], v[72:73], -2.0, 1.0 op_sel_hi:[1,0,0]
	v_pk_fma_f32 v[74:75], v[74:75], -2.0, 1.0 op_sel_hi:[1,0,0]
	v_pk_fma_f32 v[76:77], v[76:77], -2.0, 1.0 op_sel_hi:[1,0,0]
	v_pk_fma_f32 v[78:79], v[78:79], -2.0, 1.0 op_sel_hi:[1,0,0]
	v_pk_fma_f32 v[80:81], v[80:81], -2.0, 1.0 op_sel_hi:[1,0,0]
	v_pk_fma_f32 v[82:83], v[82:83], -2.0, 1.0 op_sel_hi:[1,0,0]
	v_pk_fma_f32 v[84:85], v[84:85], -2.0, 1.0 op_sel_hi:[1,0,0]
	v_pk_fma_f32 v[86:87], v[86:87], -2.0, 1.0 op_sel_hi:[1,0,0]
	v_pk_fma_f32 v[88:89], v[88:89], -2.0, 1.0 op_sel_hi:[1,0,0]
	v_pk_fma_f32 v[90:91], v[90:91], -2.0, 1.0 op_sel_hi:[1,0,0]
	v_pk_fma_f32 v[92:93], v[92:93], -2.0, 1.0 op_sel_hi:[1,0,0]
	v_pk_fma_f32 v[94:95], v[94:95], -2.0, 1.0 op_sel_hi:[1,0,0]
	v_pk_fma_f32 v[96:97], v[96:97], -2.0, 1.0 op_sel_hi:[1,0,0]
	v_pk_fma_f32 v[98:99], v[98:99], -2.0, 1.0 op_sel_hi:[1,0,0]
	v_pk_fma_f32 v[100:101], v[100:101], -2.0, 1.0 op_sel_hi:[1,0,0]
	ds_write_b128 v214, v[66:69]
	ds_write_b128 v214, v[70:73] offset:64
	ds_write_b128 v214, v[74:77] offset:128
	ds_write_b128 v214, v[78:81] offset:192
	ds_write_b128 v214, v[82:85] offset:256
	ds_write_b128 v214, v[86:89] offset:320
	ds_write_b128 v214, v[90:93] offset:384
	ds_write_b128 v214, v[94:97] offset:448
	v_pk_fma_f32 v[102:103], v[102:103], -2.0, 1.0 op_sel_hi:[1,0,0]
	v_pk_fma_f32 v[104:105], v[104:105], -2.0, 1.0 op_sel_hi:[1,0,0]
	v_pk_fma_f32 v[108:109], v[108:109], -2.0, 1.0 op_sel_hi:[1,0,0]
	v_pk_fma_f32 v[110:111], v[110:111], -2.0, 1.0 op_sel_hi:[1,0,0]
	v_pk_fma_f32 v[112:113], v[112:113], -2.0, 1.0 op_sel_hi:[1,0,0]
	v_pk_fma_f32 v[114:115], v[114:115], -2.0, 1.0 op_sel_hi:[1,0,0]
	v_pk_fma_f32 v[116:117], v[116:117], -2.0, 1.0 op_sel_hi:[1,0,0]
	v_pk_fma_f32 v[118:119], v[118:119], -2.0, 1.0 op_sel_hi:[1,0,0]
	v_pk_fma_f32 v[120:121], v[120:121], -2.0, 1.0 op_sel_hi:[1,0,0]
	v_pk_fma_f32 v[122:123], v[122:123], -2.0, 1.0 op_sel_hi:[1,0,0]
	v_pk_fma_f32 v[124:125], v[124:125], -2.0, 1.0 op_sel_hi:[1,0,0]
	v_pk_fma_f32 v[126:127], v[126:127], -2.0, 1.0 op_sel_hi:[1,0,0]
	v_pk_fma_f32 v[128:129], v[128:129], -2.0, 1.0 op_sel_hi:[1,0,0]
	v_pk_fma_f32 v[130:131], v[130:131], -2.0, 1.0 op_sel_hi:[1,0,0]
	ds_read_b128 v[66:69], v215
	ds_read_b128 v[70:73], v215 offset:1056
	ds_read_b128 v[74:77], v215 offset:2112
	ds_read_b128 v[78:81], v215 offset:3168
	ds_read_b128 v[82:85], v215 offset:4224
	ds_read_b128 v[86:89], v215 offset:5280
	ds_read_b128 v[90:93], v215 offset:6336
	ds_read_b128 v[94:97], v215 offset:7392
	ds_write_b128 v214, v[98:101]
	ds_write_b128 v214, v[102:105] offset:64
	ds_write_b128 v214, v[108:111] offset:128
	ds_write_b128 v214, v[112:115] offset:192
	ds_write_b128 v214, v[116:119] offset:256
	ds_write_b128 v214, v[120:123] offset:320
	ds_write_b128 v214, v[124:127] offset:384
	ds_write_b128 v214, v[128:131] offset:448
	ds_read_b128 v[98:101], v215
	ds_read_b128 v[102:105], v215 offset:1056
	ds_read_b128 v[108:111], v215 offset:2112
	ds_read_b128 v[112:115], v215 offset:3168
	ds_read_b128 v[116:119], v215 offset:4224
	ds_read_b128 v[120:123], v215 offset:5280
	ds_read_b128 v[124:127], v215 offset:6336
	ds_read_b128 v[128:131], v215 offset:7392
	v_add_u32_e32 v137, 0x14000, v132
	v_add_u32_e32 v138, 0x18000, v132
	v_add_u32_e32 v139, 0x1c000, v132
	s_waitcnt lgkmcnt(14)
	buffer_store_dwordx4 v[66:69], v132, s[8:11], 0 offen sc0 nt sc1
	buffer_store_dwordx4 v[70:73], v133, s[8:11], 0 offen sc0 nt sc1
	buffer_store_dwordx4 v[74:77], v134, s[8:11], 0 offen sc0 nt sc1
	buffer_store_dwordx4 v[78:81], v135, s[8:11], 0 offen sc0 nt sc1
	buffer_store_dwordx4 v[82:85], v136, s[8:11], 0 offen sc0 nt sc1
	buffer_store_dwordx4 v[86:89], v137, s[8:11], 0 offen sc0 nt sc1
	buffer_store_dwordx4 v[90:93], v138, s[8:11], 0 offen sc0 nt sc1
	buffer_store_dwordx4 v[94:97], v139, s[8:11], 0 offen sc0 nt sc1
	s_waitcnt lgkmcnt(7)
	buffer_store_dwordx4 v[98:101], v132, s[8:11], 0 offen offset:512 sc0 nt sc1
	s_waitcnt lgkmcnt(6)
	buffer_store_dwordx4 v[102:105], v133, s[8:11], 0 offen offset:512 sc0 nt sc1
	s_waitcnt lgkmcnt(5)
	buffer_store_dwordx4 v[108:111], v134, s[8:11], 0 offen offset:512 sc0 nt sc1
	s_waitcnt lgkmcnt(4)
	buffer_store_dwordx4 v[112:115], v135, s[8:11], 0 offen offset:512 sc0 nt sc1
	s_waitcnt lgkmcnt(3)
	buffer_store_dwordx4 v[116:119], v136, s[8:11], 0 offen offset:512 sc0 nt sc1
	s_waitcnt lgkmcnt(2)
	buffer_store_dwordx4 v[120:123], v137, s[8:11], 0 offen offset:512 sc0 nt sc1
	s_waitcnt lgkmcnt(1)
	buffer_store_dwordx4 v[124:127], v138, s[8:11], 0 offen offset:512 sc0 nt sc1
	s_waitcnt lgkmcnt(0)
	buffer_store_dwordx4 v[128:131], v139, s[8:11], 0 offen offset:512 sc0 nt sc1
	s_cbranch_scc0 .LBB0_3
	s_endpgm
